# speedup vs baseline: 1.0070x; 1.0070x over previous
.LBB4_59:
	s_or_b64 exec, exec, s[2:3]
	v_bfe_u32 v102, v0, 4, 2
	v_and_b32_e32 v2, 16, v0
	v_lshlrev_b32_e32 v134, 2, v102
	s_lshl_b32 s33, s26, 5
	v_add_u32_e32 v3, 12, v134
	v_cmp_eq_u32_e32 vcc, 0, v2
	s_add_i32 s33, s33, s13
	v_mov_b32_e32 v4, 0
	v_cndmask_b32_e32 v2, v3, v134, vcc
	v_or_b32_e32 v2, s33, v2
	v_ashrrev_i32_e32 v3, 31, v2
	s_waitcnt lgkmcnt(0)
	v_lshl_add_u64 v[34:35], v[2:3], 1, s[4:5]
	s_waitcnt vmcnt(0)
	v_cmp_lt_i32_e64 s[2:3], -1, v125
	v_mov_b32_e32 v188, 0
	v_mov_b32_e32 v189, 0
	v_mov_b32_e32 v190, 0
	v_mov_b32_e32 v191, 0
	s_and_saveexec_b64 s[94:95], s[2:3]
	s_cbranch_execz .Lyp_0
	v_lshlrev_b32_e32 v228, 11, v125
	v_and_b32_e32 v228, 0xfff800, v228
	v_mov_b32_e32 v229, 0
	v_lshl_add_u64 v[228:229], v[34:35], 0, v[228:229]
	global_load_dwordx4 v[188:191], v[228:229], off
.Lyp_0:
	s_or_b64 exec, exec, s[94:95]
	v_cmp_lt_i32_e64 s[4:5], -1, v124
	v_mov_b32_e32 v192, 0
	v_mov_b32_e32 v193, 0
	v_mov_b32_e32 v194, 0
	v_mov_b32_e32 v195, 0
	s_and_saveexec_b64 s[94:95], s[4:5]
	s_cbranch_execz .Lyp_1
	v_lshlrev_b32_e32 v228, 11, v124
	v_and_b32_e32 v228, 0xfff800, v228
	v_mov_b32_e32 v229, 0
	v_lshl_add_u64 v[228:229], v[34:35], 0, v[228:229]
	global_load_dwordx4 v[192:195], v[228:229], off
.Lyp_1:
	s_or_b64 exec, exec, s[94:95]
	v_cmp_lt_i32_e64 s[6:7], -1, v127
	v_mov_b32_e32 v196, 0
	v_mov_b32_e32 v197, 0
	v_mov_b32_e32 v198, 0
	v_mov_b32_e32 v199, 0
	s_and_saveexec_b64 s[94:95], s[6:7]
	s_cbranch_execz .Lyp_2
	v_lshlrev_b32_e32 v228, 11, v127
	v_and_b32_e32 v228, 0xfff800, v228
	v_mov_b32_e32 v229, 0
	v_lshl_add_u64 v[228:229], v[34:35], 0, v[228:229]
	global_load_dwordx4 v[196:199], v[228:229], off
.Lyp_2:
	s_or_b64 exec, exec, s[94:95]
	v_cmp_lt_i32_e64 s[8:9], -1, v126
	v_mov_b32_e32 v200, 0
	v_mov_b32_e32 v201, 0
	v_mov_b32_e32 v202, 0
	v_mov_b32_e32 v203, 0
	s_and_saveexec_b64 s[94:95], s[8:9]
	s_cbranch_execz .Lyp_3
	v_lshlrev_b32_e32 v228, 11, v126
	v_and_b32_e32 v228, 0xfff800, v228
	v_mov_b32_e32 v229, 0
	v_lshl_add_u64 v[228:229], v[34:35], 0, v[228:229]
	global_load_dwordx4 v[200:203], v[228:229], off
.Lyp_3:
	s_or_b64 exec, exec, s[94:95]
	v_cmp_lt_i32_e64 s[10:11], -1, v129
	v_mov_b32_e32 v204, 0
	v_mov_b32_e32 v205, 0
	v_mov_b32_e32 v206, 0
	v_mov_b32_e32 v207, 0
	s_and_saveexec_b64 s[94:95], s[10:11]
	s_cbranch_execz .Lyp_4
	v_lshlrev_b32_e32 v228, 11, v129
	v_and_b32_e32 v228, 0xfff800, v228
	v_mov_b32_e32 v229, 0
	v_lshl_add_u64 v[228:229], v[34:35], 0, v[228:229]
	global_load_dwordx4 v[204:207], v[228:229], off
.Lyp_4:
	s_or_b64 exec, exec, s[94:95]
	v_cmp_lt_i32_e64 s[12:13], -1, v128
	v_mov_b32_e32 v208, 0
	v_mov_b32_e32 v209, 0
	v_mov_b32_e32 v210, 0
	v_mov_b32_e32 v211, 0
	s_and_saveexec_b64 s[94:95], s[12:13]
	s_cbranch_execz .Lyp_5
	v_lshlrev_b32_e32 v228, 11, v128
	v_and_b32_e32 v228, 0xfff800, v228
	v_mov_b32_e32 v229, 0
	v_lshl_add_u64 v[228:229], v[34:35], 0, v[228:229]
	global_load_dwordx4 v[208:211], v[228:229], off
.Lyp_5:
	s_or_b64 exec, exec, s[94:95]
	v_cmp_lt_i32_e64 s[16:17], -1, v131
	v_mov_b32_e32 v212, 0
	v_mov_b32_e32 v213, 0
	v_mov_b32_e32 v214, 0
	v_mov_b32_e32 v215, 0
	s_and_saveexec_b64 s[94:95], s[16:17]
	s_cbranch_execz .Lyp_6
	v_lshlrev_b32_e32 v228, 11, v131
	v_and_b32_e32 v228, 0xfff800, v228
	v_mov_b32_e32 v229, 0
	v_lshl_add_u64 v[228:229], v[34:35], 0, v[228:229]
	global_load_dwordx4 v[212:215], v[228:229], off
.Lyp_6:
	s_or_b64 exec, exec, s[94:95]
	v_cmp_lt_i32_e64 s[18:19], -1, v130
	v_mov_b32_e32 v216, 0
	v_mov_b32_e32 v217, 0
	v_mov_b32_e32 v218, 0
	v_mov_b32_e32 v219, 0
	s_and_saveexec_b64 s[94:95], s[18:19]
	s_cbranch_execz .Lyp_7
	v_lshlrev_b32_e32 v228, 11, v130
	v_and_b32_e32 v228, 0xfff800, v228
	v_mov_b32_e32 v229, 0
	v_lshl_add_u64 v[228:229], v[34:35], 0, v[228:229]
	global_load_dwordx4 v[216:219], v[228:229], off
.Lyp_7:
	s_or_b64 exec, exec, s[94:95]
	v_cmp_lt_i32_e64 s[20:21], -1, v133
	v_mov_b32_e32 v220, 0
	v_mov_b32_e32 v221, 0
	v_mov_b32_e32 v222, 0
	v_mov_b32_e32 v223, 0
	s_and_saveexec_b64 s[94:95], s[20:21]
	s_cbranch_execz .Lyp_8
	v_lshlrev_b32_e32 v228, 11, v133
	v_and_b32_e32 v228, 0xfff800, v228
	v_mov_b32_e32 v229, 0
	v_lshl_add_u64 v[228:229], v[34:35], 0, v[228:229]
	global_load_dwordx4 v[220:223], v[228:229], off
.Lyp_8:
	s_or_b64 exec, exec, s[94:95]
	v_cmp_lt_i32_e64 s[22:23], -1, v132
	v_mov_b32_e32 v224, 0
	v_mov_b32_e32 v225, 0
	v_mov_b32_e32 v226, 0
	v_mov_b32_e32 v227, 0
	s_and_saveexec_b64 s[94:95], s[22:23]
	s_cbranch_execz .Lyp_9
	v_lshlrev_b32_e32 v228, 11, v132
	v_and_b32_e32 v228, 0xfff800, v228
	v_mov_b32_e32 v229, 0
	v_lshl_add_u64 v[228:229], v[34:35], 0, v[228:229]
	global_load_dwordx4 v[224:227], v[228:229], off
.Lyp_9:
	s_or_b64 exec, exec, s[94:95]
	s_waitcnt vmcnt(0)
	v_mov_b32_e32 v43, v188
	v_mov_b32_e32 v6, v189
	v_mov_b32_e32 v8, v190
	v_mov_b32_e32 v9, v191
	v_mov_b32_e32 v2, v192
	v_mov_b32_e32 v3, v193
	v_mov_b32_e32 v4, v194
	v_mov_b32_e32 v5, v195
	v_mov_b32_e32 v14, v196
	v_mov_b32_e32 v7, v197
	v_mov_b32_e32 v16, v198
	v_mov_b32_e32 v17, v199
	v_mov_b32_e32 v10, v200
	v_mov_b32_e32 v11, v201
	v_mov_b32_e32 v12, v202
	v_mov_b32_e32 v13, v203
	v_mov_b32_e32 v22, v204
	v_mov_b32_e32 v15, v205
	v_mov_b32_e32 v24, v206
	v_mov_b32_e32 v25, v207
	v_mov_b32_e32 v18, v208
	v_mov_b32_e32 v19, v209
	v_mov_b32_e32 v20, v210
	v_mov_b32_e32 v21, v211
	v_mov_b32_e32 v90, v212
	v_mov_b32_e32 v30, v213
	v_mov_b32_e32 v32, v214
	v_mov_b32_e32 v33, v215
	v_mov_b32_e32 v26, v216
	v_mov_b32_e32 v27, v217
	v_mov_b32_e32 v28, v218
	v_mov_b32_e32 v29, v219
	v_mov_b32_e32 v38, v220
	v_mov_b32_e32 v39, v221
	v_mov_b32_e32 v40, v222
	v_mov_b32_e32 v41, v223
	v_mov_b32_e32 v103, v224
	v_mov_b32_e32 v104, v225
	v_mov_b32_e32 v36, v226
	v_mov_b32_e32 v37, v227
	v_permlane16_swap_b32_e32 v43, v8
	v_permlane16_swap_b32_e32 v6, v9
	v_permlane16_swap_b32_e32 v2, v4
	v_permlane16_swap_b32_e32 v3, v5
	v_permlane16_swap_b32_e32 v14, v16
	v_permlane16_swap_b32_e32 v7, v17
	v_permlane16_swap_b32_e32 v10, v12
	v_permlane16_swap_b32_e32 v11, v13
	v_permlane16_swap_b32_e32 v22, v24
	v_permlane16_swap_b32_e32 v15, v25
	v_permlane16_swap_b32_e32 v18, v20
	v_permlane16_swap_b32_e32 v19, v21
	v_permlane16_swap_b32_e32 v90, v32
	v_permlane16_swap_b32_e32 v30, v33
	v_permlane16_swap_b32_e32 v26, v28
	v_permlane16_swap_b32_e32 v27, v29
	v_permlane16_swap_b32_e32 v38, v40
	v_permlane16_swap_b32_e32 v39, v41
	v_permlane16_swap_b32_e32 v103, v36
	v_permlane16_swap_b32_e32 v104, v37
	s_mov_b64 s[24:25], -1
	s_and_b64 vcc, exec, s[30:31]
	s_cbranch_vccnz .LBB4_182
	s_andn2_b64 vcc, exec, s[24:25]
	s_cbranch_vccz .LBB4_183

	.amdhsa_kernel _Z8moe_gemmILi2EEvPKDF16_S1_PvPKyPKiPKfS1_
		.amdhsa_group_segment_fixed_size 0
		.amdhsa_private_segment_fixed_size 0
		.amdhsa_kernarg_size 56
		.amdhsa_user_sgpr_count 2
		.amdhsa_user_sgpr_dispatch_ptr 0
		.amdhsa_user_sgpr_queue_ptr 0
		.amdhsa_user_sgpr_kernarg_segment_ptr 1
		.amdhsa_user_sgpr_dispatch_id 0
		.amdhsa_user_sgpr_kernarg_preload_length 0
		.amdhsa_user_sgpr_kernarg_preload_offset 0
		.amdhsa_user_sgpr_private_segment_size 0
		.amdhsa_uses_dynamic_stack 0
		.amdhsa_enable_private_segment 0
		.amdhsa_system_sgpr_workgroup_id_x 1
		.amdhsa_system_sgpr_workgroup_id_y 0
		.amdhsa_system_sgpr_workgroup_id_z 0
		.amdhsa_system_sgpr_workgroup_info 0
		.amdhsa_system_vgpr_workitem_id 0
		.amdhsa_next_free_vgpr 232
		.amdhsa_next_free_sgpr 96
		.amdhsa_accum_offset 232
		.amdhsa_reserve_vcc 1
		.amdhsa_float_round_mode_32 0
		.amdhsa_float_round_mode_16_64 0
		.amdhsa_float_denorm_mode_32 3
		.amdhsa_float_denorm_mode_16_64 3
		.amdhsa_dx10_clamp 1
		.amdhsa_ieee_mode 1
		.amdhsa_fp16_overflow 0
		.amdhsa_tg_split 0
		.amdhsa_exception_fp_ieee_invalid_op 0
		.amdhsa_exception_fp_denorm_src 0
		.amdhsa_exception_fp_ieee_div_zero 0
		.amdhsa_exception_fp_ieee_overflow 0
		.amdhsa_exception_fp_ieee_underflow 0
		.amdhsa_exception_fp_ieee_inexact 0
		.amdhsa_exception_int_div_zero 0
	.end_amdhsa_kernel

amdhsa.kernels:
  - .agpr_count:     0
    .args:
      - .actual_access:  write_only
        .address_space:  global
        .offset:         0
        .size:           8
        .value_kind:     global_buffer
    .group_segment_fixed_size: 0
    .kernarg_segment_align: 8
    .kernarg_segment_size: 8
    .language:       OpenCL C
    .language_version:
      - 2
      - 0
    .max_flat_workgroup_size: 1024
    .name:           _Z15zero_cnt_kernelPy
    .private_segment_fixed_size: 0
    .sgpr_count:     10
    .sgpr_spill_count: 0
    .symbol:         _Z15zero_cnt_kernelPy.kd
    .uniform_work_group_size: 1
    .uses_dynamic_stack: false
    .vgpr_count:     3
    .vgpr_spill_count: 0
    .wavefront_size: 64
  - .agpr_count:     0
    .args:
      - .actual_access:  read_only
        .address_space:  global
        .offset:         0
        .size:           8
        .value_kind:     global_buffer
      - .actual_access:  read_only
        .address_space:  global
        .offset:         8
        .size:           8
        .value_kind:     global_buffer
      - .actual_access:  read_only
        .address_space:  global
        .offset:         16
        .size:           8
        .value_kind:     global_buffer
      - .actual_access:  read_only
        .address_space:  global
        .offset:         24
        .size:           8
        .value_kind:     global_buffer
      - .actual_access:  write_only
        .address_space:  global
        .offset:         32
        .size:           8
        .value_kind:     global_buffer
      - .actual_access:  write_only
        .address_space:  global
        .offset:         40
        .size:           8
        .value_kind:     global_buffer
      - .actual_access:  write_only
        .address_space:  global
        .offset:         48
        .size:           8
        .value_kind:     global_buffer
      - .address_space:  global
        .offset:         56
        .size:           8
        .value_kind:     global_buffer
      - .actual_access:  write_only
        .address_space:  global
        .offset:         64
        .size:           8
        .value_kind:     global_buffer
      - .actual_access:  write_only
        .address_space:  global
        .offset:         72
        .size:           8
        .value_kind:     global_buffer
    .group_segment_fixed_size: 0
    .kernarg_segment_align: 8
    .kernarg_segment_size: 80
    .language:       OpenCL C
    .language_version:
      - 2
      - 0
    .max_flat_workgroup_size: 256
    .name:           _Z11prep_kernelPKfS0_S0_S0_PDF16_S1_S1_PyPiPf
    .private_segment_fixed_size: 0
    .sgpr_count:     55
    .sgpr_spill_count: 0
    .symbol:         _Z11prep_kernelPKfS0_S0_S0_PDF16_S1_S1_PyPiPf.kd
    .uniform_work_group_size: 1
    .uses_dynamic_stack: false
    .vgpr_count:     248
    .vgpr_spill_count: 0
    .wavefront_size: 64
  - .agpr_count:     0
    .args:
      - .address_space:  global
        .offset:         0
        .size:           8
        .value_kind:     global_buffer
      - .address_space:  global
        .offset:         8
        .size:           8
        .value_kind:     global_buffer
      - .actual_access:  write_only
        .address_space:  global
        .offset:         16
        .size:           8
        .value_kind:     global_buffer
      - .actual_access:  read_only
        .address_space:  global
        .offset:         24
        .size:           8
        .value_kind:     global_buffer
      - .actual_access:  read_only
        .address_space:  global
        .offset:         32
        .size:           8
        .value_kind:     global_buffer
      - .actual_access:  read_only
        .address_space:  global
        .offset:         40
        .size:           8
        .value_kind:     global_buffer
      - .actual_access:  read_only
        .address_space:  global
        .offset:         48
        .size:           8
        .value_kind:     global_buffer
    .group_segment_fixed_size: 0
    .kernarg_segment_align: 8
    .kernarg_segment_size: 56
    .language:       OpenCL C
    .language_version:
      - 2
      - 0
    .max_flat_workgroup_size: 512
    .name:           _Z8moe_gemmILi0EEvPKDF16_S1_PvPKyPKiPKfS1_
    .private_segment_fixed_size: 0
    .sgpr_count:     98
    .sgpr_spill_count: 0
    .symbol:         _Z8moe_gemmILi0EEvPKDF16_S1_PvPKyPKiPKfS1_.kd
    .uniform_work_group_size: 1
    .uses_dynamic_stack: false
    .vgpr_count:     256
    .vgpr_spill_count: 0
    .wavefront_size: 64
  - .agpr_count:     0
    .args:
      - .address_space:  global
        .offset:         0
        .size:           8
        .value_kind:     global_buffer
      - .address_space:  global
        .offset:         8
        .size:           8
        .value_kind:     global_buffer
      - .actual_access:  write_only
        .address_space:  global
        .offset:         16
        .size:           8
        .value_kind:     global_buffer
      - .actual_access:  read_only
        .address_space:  global
        .offset:         24
        .size:           8
        .value_kind:     global_buffer
      - .actual_access:  read_only
        .address_space:  global
        .offset:         32
        .size:           8
        .value_kind:     global_buffer
      - .actual_access:  read_only
        .address_space:  global
        .offset:         40
        .size:           8
        .value_kind:     global_buffer
      - .actual_access:  read_only
        .address_space:  global
        .offset:         48
        .size:           8
        .value_kind:     global_buffer
    .group_segment_fixed_size: 0
    .kernarg_segment_align: 8
    .kernarg_segment_size: 56
    .language:       OpenCL C
    .language_version:
      - 2
      - 0
    .max_flat_workgroup_size: 512
    .name:           _Z8moe_gemmILi1EEvPKDF16_S1_PvPKyPKiPKfS1_
    .private_segment_fixed_size: 0
    .sgpr_count:     100
    .sgpr_spill_count: 0
    .symbol:         _Z8moe_gemmILi1EEvPKDF16_S1_PvPKyPKiPKfS1_.kd
    .uniform_work_group_size: 1
    .uses_dynamic_stack: false
    .vgpr_count:     180
    .vgpr_spill_count: 0
    .wavefront_size: 64
  - .agpr_count:     0
    .args:
      - .address_space:  global
        .offset:         0
        .size:           8
        .value_kind:     global_buffer
      - .address_space:  global
        .offset:         8
        .size:           8
        .value_kind:     global_buffer
      - .actual_access:  write_only
        .address_space:  global
        .offset:         16
        .size:           8
        .value_kind:     global_buffer
      - .actual_access:  read_only
        .address_space:  global
        .offset:         24
        .size:           8
        .value_kind:     global_buffer
      - .actual_access:  read_only
        .address_space:  global
        .offset:         32
        .size:           8
        .value_kind:     global_buffer
      - .actual_access:  read_only
        .address_space:  global
        .offset:         40
        .size:           8
        .value_kind:     global_buffer
      - .actual_access:  read_only
        .address_space:  global
        .offset:         48
        .size:           8
        .value_kind:     global_buffer
    .group_segment_fixed_size: 0
    .kernarg_segment_align: 8
    .kernarg_segment_size: 56
    .language:       OpenCL C
    .language_version:
      - 2
      - 0
    .max_flat_workgroup_size: 512
    .name:           _Z8moe_gemmILi2EEvPKDF16_S1_PvPKyPKiPKfS1_
    .private_segment_fixed_size: 0
    .sgpr_count:     102
    .sgpr_spill_count: 0
    .symbol:         _Z8moe_gemmILi2EEvPKDF16_S1_PvPKyPKiPKfS1_.kd
    .uniform_work_group_size: 1
    .uses_dynamic_stack: false
    .vgpr_count:     232
    .vgpr_spill_count: 0
    .wavefront_size: 64
